# QKV GEMM phases: workgroups with blockIdx bit 2 set start ~8 us late (two s_sleep 127) so the halves' epilogue store bursts interleave
# speedup vs baseline: 1.0010x; 1.0001x over previous
.LBB0_225:
	s_add_u32 s4, s90, 0x300000
	s_addc_u32 s5, s91, 0
	s_cmp_lt_i32 s12, 2
	s_cselect_b64 s[0:1], -1, 0
	s_cmp_gt_i32 s13, 1
	s_cselect_b64 s[2:3], -1, 0
	s_and_b64 s[0:1], s[0:1], s[2:3]
	s_andn2_b64 vcc, exec, s[0:1]
	s_cbranch_vccnz .LBB0_301
	v_readlane_b32 s32, v254, 0
	s_nop 3
	s_bitcmp1_b32 s32, 2
	s_cbranch_scc0 .Lstag_0
	s_sleep 127
	s_sleep 127
.Lstag_0:
	v_readlane_b32 s0, v254, 5
	s_andn2_b32 s0, s0, 63
	v_readlane_b32 s1, v254, 0
	s_cmpk_gt_i32 s1, 0x5ff
	s_mov_b32 s1, -1
	s_waitcnt vmcnt(2)
	v_mbcnt_lo_u32_b32 v0, s1, 0
	v_mbcnt_hi_u32_b32 v0, s1, v0
	v_add_u32_e32 v8, s0, v0
	s_nop 0
	v_readfirstlane_b32 s3, v8
	s_cbranch_scc1 .LBB0_247
	v_lshlrev_b32_e32 v0, 4, v8
	v_add_u32_e32 v1, 0x2000, v0
	v_ashrrev_i32_e32 v2, 31, v1
	v_lshrrev_b32_e32 v2, 22, v2
	v_add_u32_e32 v2, v1, v2
	v_ashrrev_i32_e32 v2, 10, v2
	v_mul_i32_i24_e32 v3, 0x400, v2
	v_sub_u32_e32 v1, v1, v3
	v_lshrrev_b32_e32 v3, 4, v1
	v_bitop3_b32 v1, v3, v1, 32 bitop3:0x6c
	v_ashrrev_i32_e32 v3, 31, v1
	v_lshrrev_b32_e32 v3, 26, v3
	v_add_u32_e32 v3, v1, v3
	s_waitcnt vmcnt(1)
	v_lshlrev_b32_e32 v5, 3, v2
	v_ashrrev_i32_e32 v4, 6, v3
	v_and_b32_e32 v5, -16, v5
	v_and_b32_e32 v3, 0xc0, v3
	v_add_u32_e32 v5, v4, v5
	v_and_b32_e32 v4, 3, v4
	s_mov_b32 s0, 0x3fffe0
	v_sub_u32_e32 v1, v1, v3
	v_mov_b32_e32 v3, 1
	v_and_or_b32 v4, v5, s0, v4
	v_lshrrev_b32_e32 v6, 2, v5
	v_lshlrev_b32_e32 v5, 1, v5
	v_lshlrev_b32_e32 v2, 5, v2
	v_ashrrev_i16_sdwa v1, v3, sext(v1) dst_sel:DWORD dst_unused:UNUSED_PAD src0_sel:DWORD src1_sel:BYTE_0
	v_and_b32_e32 v6, 4, v6
	v_and_b32_e32 v5, 24, v5
	v_and_b32_e32 v2, 32, v2
	v_bfe_i32 v1, v1, 0, 16
	v_or3_b32 v4, v4, v6, v5
	v_add_lshl_u32 v1, v2, v1, 1
	v_lshl_add_u32 v160, v4, 10, v1
	v_bfe_i32 v1, v8, 27, 1
	v_lshrrev_b32_e32 v1, 22, v1
	v_add_u32_e32 v1, v0, v1
	v_and_b32_e32 v1, 0xfffffc00, v1
	v_sub_u32_e32 v0, v0, v1
	v_lshrrev_b32_e32 v1, 4, v0
	v_ashrrev_i32_e32 v4, 31, v8
	v_bitop3_b32 v0, v1, v0, 32 bitop3:0x6c
	v_lshrrev_b32_e32 v4, 26, v4
	v_ashrrev_i32_e32 v1, 31, v0
	v_add_u32_e32 v4, v8, v4
	v_lshrrev_b32_e32 v1, 26, v1
	v_ashrrev_i32_e32 v4, 6, v4
	v_add_u32_e32 v1, v0, v1
	v_lshlrev_b32_e32 v5, 3, v4
	s_add_u32 s16, s90, 0x800000
	v_readlane_b32 s2, v254, 0
	v_ashrrev_i32_e32 v2, 6, v1
	v_and_b32_e32 v5, -16, v5
	v_and_b32_e32 v1, 0xc0, v1
	s_addc_u32 s17, s91, 0
	s_ashr_i32 s18, s2, 31
	v_add_u32_e32 v5, v2, v5
	v_and_b32_e32 v2, 3, v2
	v_sub_u32_e32 v0, v0, v1
	v_and_or_b32 v2, v5, s0, v2
	v_lshrrev_b32_e32 v6, 2, v5
	v_lshlrev_b32_e32 v5, 1, v5
	v_lshlrev_b32_e32 v4, 5, v4
	v_ashrrev_i16_sdwa v0, v3, sext(v0) dst_sel:DWORD dst_unused:UNUSED_PAD src0_sel:DWORD src1_sel:BYTE_0
	s_lshr_b32 s0, s18, 29
	v_and_b32_e32 v6, 4, v6
	v_and_b32_e32 v5, 24, v5
	v_and_b32_e32 v4, 32, v4
	v_bfe_i32 v0, v0, 0, 16
	s_add_i32 s0, s2, s0
	s_ashr_i32 s8, s3, 6
	v_or3_b32 v2, v2, v6, v5
	v_add_lshl_u32 v0, v4, v0, 1
	s_ashr_i32 s1, s0, 3
	s_and_b32 s0, s0, -8
	s_ashr_i32 s10, s3, 8
	s_lshl_b32 s9, s8, 10
	v_lshl_add_u32 v162, v2, 10, v0
	s_sub_i32 s0, s2, s0
	v_mov_b32_e32 v0, v8
	s_cmp_lt_i32 s0, 0
	s_movk_i32 s19, 0xc1
	s_cselect_b32 s2, s19, 0xc0
	v_ashrrev_i32_e32 v2, 31, v0
	v_lshrrev_b32_e32 v2, 26, v2
	s_mul_i32 s0, s2, s0
	v_lshlrev_b32_e32 v1, 4, v0
	v_add_u32_e32 v2, v0, v2
	v_bfe_i32 v0, v0, 27, 1
	s_add_i32 s0, s0, s1
	v_lshrrev_b32_e32 v0, 22, v0
	s_mul_hi_i32 s1, s0, 0x2aaaaaab
	v_add_u32_e32 v0, v1, v0
	s_lshr_b32 s2, s1, 31
	s_ashr_i32 s1, s1, 4
	v_and_b32_e32 v0, 0xfffffc00, v0
	s_add_i32 s1, s1, s2
	v_sub_u32_e32 v0, v1, v0
	s_lshl_b32 s6, s1, 3
	s_mulk_i32 s1, 0x60
	v_ashrrev_i32_e32 v9, 6, v2
	v_lshrrev_b32_e32 v2, 4, v0
	s_sub_i32 s0, s0, s1
	v_bitop3_b32 v0, v2, v0, 32 bitop3:0x6c
	s_bfe_i32 s1, s0, 0x80000
	v_ashrrev_i32_e32 v4, 31, v0
	s_bfe_u32 s1, s1, 0x3000c
	v_lshrrev_b32_e32 v4, 26, v4
	s_add_i32 s1, s0, s1
	v_add_u32_e32 v4, v0, v4
	s_bfe_i32 s2, s1, 0x80000
	s_and_b32 s1, s1, 0xf8
	v_ashrrev_i32_e32 v10, 6, v4
	v_and_b32_e32 v4, 0xc0, v4
	v_add_u32_e32 v1, 0x2000, v1
	s_sub_i32 s0, s0, s1
	v_sub_u32_e32 v0, v0, v4
	v_ashrrev_i32_e32 v4, 31, v1
	s_sext_i32_i16 s2, s2
	s_sext_i32_i8 s0, s0
	v_lshrrev_b32_e32 v4, 22, v4
	s_lshr_b32 s2, s2, 3
	s_add_i32 s0, s6, s0
	v_add_u32_e32 v4, v1, v4
	v_ashrrev_i32_e32 v12, 10, v4
	s_ashr_i32 s1, s0, 31
	s_bfe_i64 s[12:13], s[2:3], 0x100000
	v_mul_i32_i24_e32 v4, 0x400, v12
	s_lshl_b64 s[6:7], s[0:1], 18
	s_lshl_b64 s[12:13], s[12:13], 18
	v_sub_u32_e32 v1, v1, v4
	s_add_u32 s42, s16, s12
	v_lshlrev_b32_e32 v5, 5, v9
	v_ashrrev_i16_sdwa v0, v3, sext(v0) dst_sel:DWORD dst_unused:UNUSED_PAD src0_sel:DWORD src1_sel:BYTE_0
	v_lshrrev_b32_e32 v4, 4, v1
	s_addc_u32 s43, s17, s13
	s_add_i32 s20, s9, 0
	v_and_b32_e32 v5, 32, v5
	v_bfe_i32 v11, v0, 0, 16
	v_bitop3_b32 v1, v4, v1, 32 bitop3:0x6c
	s_add_i32 s21, s20, 0x10000
	s_add_i32 s22, s20, 0x12000
	v_add_u32_e32 v0, v5, v11
	v_ashrrev_i32_e32 v5, 31, v1
	s_mov_b32 m0, s21
	s_add_u32 s12, s42, 0x20000
	v_lshrrev_b32_e32 v5, 26, v5
	global_load_lds_dwordx4 v162, s[42:43]
	s_mov_b32 m0, s22
	s_addc_u32 s13, s43, 0
	s_add_i32 s23, s20, 0x14000
	v_add_u32_e32 v5, v1, v5
	global_load_lds_dwordx4 v160, s[42:43]
	s_mov_b32 m0, s23
	s_add_i32 s24, s20, 0x16000
	v_ashrrev_i32_e32 v13, 6, v5
	v_and_b32_e32 v5, 0xc0, v5
	global_load_lds_dwordx4 v162, s[12:13]
	s_mov_b32 m0, s24
	v_lshlrev_b32_e32 v2, 3, v9
	v_sub_u32_e32 v1, v1, v5
	global_load_lds_dwordx4 v160, s[12:13]
	v_readlane_b32 s12, v254, 44
	v_and_b32_e32 v2, 0x3ffff0, v2
	v_lshlrev_b32_e32 v4, 3, v12
	v_lshlrev_b32_e32 v6, 5, v12
	v_ashrrev_i16_sdwa v1, v3, sext(v1) dst_sel:DWORD dst_unused:UNUSED_PAD src0_sel:DWORD src1_sel:BYTE_0
	v_readlane_b32 s13, v254, 45
	s_add_u32 s40, s12, s6
	v_and_b32_e32 v4, 0x3ffff0, v4
	v_and_b32_e32 v6, 32, v6
	v_bfe_i32 v14, v1, 0, 16
	v_add_lshl_u32 v2, v10, v2, 10
	s_addc_u32 s41, s13, s7
	s_add_i32 s25, s20, 0x2000
	v_add_u32_e32 v1, v6, v14
	v_lshl_add_u32 v164, v0, 1, v2
	v_add_lshl_u32 v0, v13, v4, 10
	s_mov_b32 m0, s20
	s_add_u32 s6, s40, 0x20000
	v_lshl_add_u32 v166, v1, 1, v0
	global_load_lds_dwordx4 v164, s[40:41]
	s_mov_b32 m0, s25
	s_addc_u32 s7, s41, 0
	s_add_i32 s26, s20, 0x4000
	global_load_lds_dwordx4 v166, s[40:41]
	s_mov_b32 m0, s26
	s_add_i32 s27, s20, 0x6000
	global_load_lds_dwordx4 v164, s[6:7]
	s_mov_b32 m0, s27
	v_mov_b32_e32 v163, 0
	global_load_lds_dwordx4 v166, s[6:7]
	v_mov_b32_e32 v161, v163
	v_mov_b32_e32 v165, v163
	v_mov_b32_e32 v167, v163
	s_cmp_eq_u32 s10, 1
	v_lshl_add_u64 v[6:7], s[42:43], 0, v[162:163]
	v_lshl_add_u64 v[4:5], s[42:43], 0, v[160:161]
	v_lshl_add_u64 v[0:1], s[40:41], 0, v[164:165]
	s_cselect_b64 s[6:7], -1, 0
	s_cmp_lg_u32 s10, 1
	v_lshl_add_u64 v[2:3], s[40:41], 0, v[166:167]
	s_cbranch_scc1 .LBB0_229
	s_barrier

.LBB0_1164:
	s_cmp_lt_i32 s12, 12
	s_cselect_b64 s[0:1], -1, 0
	s_cmp_gt_u32 s13, 11
	s_cselect_b64 s[2:3], -1, 0
	s_and_b64 s[0:1], s[0:1], s[2:3]
	s_andn2_b64 vcc, exec, s[0:1]
	s_cbranch_vccnz .LBB0_1236
	v_readlane_b32 s32, v254, 0
	s_nop 3
	s_bitcmp1_b32 s32, 2
	s_cbranch_scc0 .Lstag_1
	s_sleep 127
	s_sleep 127
.Lstag_1:
	v_readlane_b32 s0, v254, 5
	s_andn2_b32 s0, s0, 63
	v_readlane_b32 s1, v254, 0
	s_cmpk_gt_i32 s1, 0x2ff
	s_mov_b32 s1, -1
	s_nop 0
	v_mbcnt_lo_u32_b32 v0, s1, 0
	v_mbcnt_hi_u32_b32 v0, s1, v0
	v_add_u32_e32 v8, s0, v0
	s_nop 0
	v_readfirstlane_b32 s5, v8
	s_cbranch_scc1 .LBB0_1182
	v_lshlrev_b32_e32 v0, 4, v8
	v_add_u32_e32 v1, 0x2000, v0
	v_ashrrev_i32_e32 v2, 31, v1
	v_lshrrev_b32_e32 v2, 22, v2
	v_add_u32_e32 v2, v1, v2
	v_ashrrev_i32_e32 v2, 10, v2
	v_mul_i32_i24_e32 v3, 0x400, v2
	v_sub_u32_e32 v1, v1, v3
	v_lshrrev_b32_e32 v3, 4, v1
	v_bitop3_b32 v1, v3, v1, 32 bitop3:0x6c
	v_ashrrev_i32_e32 v3, 31, v1
	v_lshrrev_b32_e32 v3, 26, v3
	v_add_u32_e32 v3, v1, v3
	s_waitcnt lgkmcnt(0)
	v_lshlrev_b32_e32 v5, 3, v2
	v_ashrrev_i32_e32 v4, 6, v3
	v_and_b32_e32 v5, -16, v5
	v_and_b32_e32 v3, 0xc0, v3
	v_add_u32_e32 v5, v4, v5
	v_and_b32_e32 v4, 3, v4
	s_mov_b32 s0, 0x3fffe0
	v_sub_u32_e32 v1, v1, v3
	v_mov_b32_e32 v3, 1
	v_and_or_b32 v4, v5, s0, v4
	v_lshrrev_b32_e32 v6, 2, v5
	v_lshlrev_b32_e32 v5, 1, v5
	v_lshlrev_b32_e32 v2, 5, v2
	v_ashrrev_i16_sdwa v1, v3, sext(v1) dst_sel:DWORD dst_unused:UNUSED_PAD src0_sel:DWORD src1_sel:BYTE_0
	v_and_b32_e32 v6, 4, v6
	v_and_b32_e32 v5, 24, v5
	v_and_b32_e32 v2, 32, v2
	v_bfe_i32 v1, v1, 0, 16
	v_or3_b32 v4, v4, v6, v5
	v_add_lshl_u32 v1, v2, v1, 1
	v_lshl_add_u32 v160, v4, 10, v1
	v_bfe_i32 v1, v8, 27, 1
	v_lshrrev_b32_e32 v1, 22, v1
	v_add_u32_e32 v1, v0, v1
	v_and_b32_e32 v1, 0xfffffc00, v1
	v_sub_u32_e32 v0, v0, v1
	v_lshrrev_b32_e32 v1, 4, v0
	v_ashrrev_i32_e32 v4, 31, v8
	v_bitop3_b32 v0, v1, v0, 32 bitop3:0x6c
	v_lshrrev_b32_e32 v4, 26, v4
	v_ashrrev_i32_e32 v1, 31, v0
	v_add_u32_e32 v4, v8, v4
	v_lshrrev_b32_e32 v1, 26, v1
	v_ashrrev_i32_e32 v4, 6, v4
	v_add_u32_e32 v1, v0, v1
	v_lshlrev_b32_e32 v5, 3, v4
	s_add_u32 s18, s90, 0x2c500000
	v_readlane_b32 s4, v254, 0
	v_ashrrev_i32_e32 v2, 6, v1
	v_and_b32_e32 v5, -16, v5
	v_and_b32_e32 v1, 0xc0, v1
	s_addc_u32 s19, s91, 0
	s_ashr_i32 s20, s4, 31
	v_add_u32_e32 v5, v2, v5
	v_and_b32_e32 v2, 3, v2
	v_sub_u32_e32 v0, v0, v1
	v_and_or_b32 v2, v5, s0, v2
	v_lshrrev_b32_e32 v6, 2, v5
	v_lshlrev_b32_e32 v5, 1, v5
	v_lshlrev_b32_e32 v4, 5, v4
	v_ashrrev_i16_sdwa v0, v3, sext(v0) dst_sel:DWORD dst_unused:UNUSED_PAD src0_sel:DWORD src1_sel:BYTE_0
	s_lshr_b32 s0, s20, 29
	v_and_b32_e32 v6, 4, v6
	v_and_b32_e32 v5, 24, v5
	v_and_b32_e32 v4, 32, v4
	v_bfe_i32 v0, v0, 0, 16
	s_add_i32 s0, s4, s0
	s_ashr_i32 s2, s5, 6
	v_or3_b32 v2, v2, v6, v5
	v_add_lshl_u32 v0, v4, v0, 1
	s_ashr_i32 s1, s0, 3
	s_and_b32 s0, s0, -8
	s_ashr_i32 s6, s5, 8
	s_lshl_b32 s3, s2, 10
	v_lshl_add_u32 v162, v2, 10, v0
	s_sub_i32 s0, s4, s0
	v_mov_b32_e32 v0, v8
	s_cmp_lt_i32 s0, 0
	s_movk_i32 s21, 0x61
	s_cselect_b32 s4, s21, 0x60
	v_ashrrev_i32_e32 v2, 31, v0
	v_lshrrev_b32_e32 v2, 26, v2
	s_mul_i32 s0, s4, s0
	v_lshlrev_b32_e32 v1, 4, v0
	v_add_u32_e32 v2, v0, v2
	v_bfe_i32 v0, v0, 27, 1
	s_add_i32 s0, s0, s1
	v_lshrrev_b32_e32 v0, 22, v0
	s_mul_hi_i32 s1, s0, 0x2aaaaaab
	v_add_u32_e32 v0, v1, v0
	s_lshr_b32 s4, s1, 31
	s_ashr_i32 s1, s1, 3
	v_and_b32_e32 v0, 0xfffffc00, v0
	s_add_i32 s1, s1, s4
	v_sub_u32_e32 v0, v1, v0
	s_lshl_b32 s7, s1, 3
	s_mul_i32 s1, s1, 48
	v_ashrrev_i32_e32 v9, 6, v2
	v_lshrrev_b32_e32 v2, 4, v0
	s_sub_i32 s0, s0, s1
	v_bitop3_b32 v0, v2, v0, 32 bitop3:0x6c
	s_bfe_i32 s1, s0, 0x80000
	v_ashrrev_i32_e32 v4, 31, v0
	s_bfe_u32 s1, s1, 0x3000c
	v_lshrrev_b32_e32 v4, 26, v4
	s_add_i32 s1, s0, s1
	v_add_u32_e32 v4, v0, v4
	s_bfe_i32 s4, s1, 0x80000
	s_and_b32 s1, s1, 0xf8
	v_ashrrev_i32_e32 v10, 6, v4
	v_and_b32_e32 v4, 0xc0, v4
	v_add_u32_e32 v1, 0x2000, v1
	s_sub_i32 s0, s0, s1
	v_sub_u32_e32 v0, v0, v4
	v_ashrrev_i32_e32 v4, 31, v1
	s_sext_i32_i16 s4, s4
	s_sext_i32_i8 s0, s0
	v_lshrrev_b32_e32 v4, 22, v4
	s_lshr_b32 s4, s4, 3
	s_add_i32 s16, s7, s0
	v_add_u32_e32 v4, v1, v4
	v_ashrrev_i32_e32 v12, 10, v4
	s_ashr_i32 s17, s16, 31
	s_bfe_i64 s[8:9], s[4:5], 0x100000
	v_mul_i32_i24_e32 v4, 0x400, v12
	s_lshl_b64 s[0:1], s[16:17], 18
	s_lshl_b64 s[8:9], s[8:9], 18
	v_sub_u32_e32 v1, v1, v4
	s_add_u32 s26, s18, s8
	v_lshlrev_b32_e32 v5, 5, v9
	v_ashrrev_i16_sdwa v0, v3, sext(v0) dst_sel:DWORD dst_unused:UNUSED_PAD src0_sel:DWORD src1_sel:BYTE_0
	v_lshrrev_b32_e32 v4, 4, v1
	s_addc_u32 s27, s19, s9
	s_add_i32 s17, s3, 0
	v_and_b32_e32 v5, 32, v5
	v_bfe_i32 v11, v0, 0, 16
	v_bitop3_b32 v1, v4, v1, 32 bitop3:0x6c
	s_add_i32 s22, s17, 0x10000
	s_add_i32 s23, s17, 0x12000
	v_add_u32_e32 v0, v5, v11
	v_ashrrev_i32_e32 v5, 31, v1
	s_mov_b32 m0, s22
	s_add_u32 s8, s26, 0x20000
	v_lshrrev_b32_e32 v5, 26, v5
	global_load_lds_dwordx4 v162, s[26:27]
	s_mov_b32 m0, s23
	s_addc_u32 s9, s27, 0
	s_add_i32 s28, s17, 0x14000
	v_add_u32_e32 v5, v1, v5
	global_load_lds_dwordx4 v160, s[26:27]
	s_mov_b32 m0, s28
	s_add_i32 s29, s17, 0x16000
	v_ashrrev_i32_e32 v13, 6, v5
	v_and_b32_e32 v5, 0xc0, v5
	global_load_lds_dwordx4 v162, s[8:9]
	s_mov_b32 m0, s29
	v_lshlrev_b32_e32 v2, 3, v9
	v_sub_u32_e32 v1, v1, v5
	global_load_lds_dwordx4 v160, s[8:9]
	v_readlane_b32 s8, v254, 44
	v_and_b32_e32 v2, 0x3ffff0, v2
	v_lshlrev_b32_e32 v4, 3, v12
	v_lshlrev_b32_e32 v6, 5, v12
	v_ashrrev_i16_sdwa v1, v3, sext(v1) dst_sel:DWORD dst_unused:UNUSED_PAD src0_sel:DWORD src1_sel:BYTE_0
	v_readlane_b32 s9, v254, 45
	s_add_u32 s24, s8, s0
	v_and_b32_e32 v4, 0x3ffff0, v4
	v_and_b32_e32 v6, 32, v6
	v_bfe_i32 v14, v1, 0, 16
	v_add_lshl_u32 v2, v10, v2, 10
	s_addc_u32 s25, s9, s1
	s_add_i32 s30, s17, 0x2000
	v_add_u32_e32 v1, v6, v14
	v_lshl_add_u32 v164, v0, 1, v2
	v_add_lshl_u32 v0, v13, v4, 10
	s_mov_b32 m0, s17
	s_add_u32 s0, s24, 0x20000
	v_lshl_add_u32 v166, v1, 1, v0
	global_load_lds_dwordx4 v164, s[24:25]
	s_mov_b32 m0, s30
	s_addc_u32 s1, s25, 0
	s_add_i32 s31, s17, 0x4000
	global_load_lds_dwordx4 v166, s[24:25]
	s_mov_b32 m0, s31
	s_add_i32 s33, s17, 0x6000
	global_load_lds_dwordx4 v164, s[0:1]
	s_mov_b32 m0, s33
	v_mov_b32_e32 v163, 0
	global_load_lds_dwordx4 v166, s[0:1]
	v_mov_b32_e32 v161, v163
	v_mov_b32_e32 v165, v163
	v_mov_b32_e32 v167, v163
	s_cmp_eq_u32 s6, 1
	v_lshl_add_u64 v[6:7], s[26:27], 0, v[162:163]
	v_lshl_add_u64 v[4:5], s[26:27], 0, v[160:161]
	v_lshl_add_u64 v[0:1], s[24:25], 0, v[164:165]
	s_cselect_b64 s[0:1], -1, 0
	s_cmp_lg_u32 s6, 1
	v_lshl_add_u64 v[2:3], s[24:25], 0, v[166:167]
	s_cbranch_scc1 .LBB0_1168
	s_barrier

.LBB0_2041:
	s_cmp_lt_i32 s12, 22
	s_cselect_b64 s[0:1], -1, 0
	s_cmp_gt_u32 s13, 21
	s_cselect_b64 s[2:3], -1, 0
	s_and_b64 s[0:1], s[0:1], s[2:3]
	s_andn2_b64 vcc, exec, s[0:1]
	s_cbranch_vccnz .LBB0_2113
	v_readlane_b32 s32, v254, 0
	s_nop 3
	s_bitcmp1_b32 s32, 2
	s_cbranch_scc0 .Lstag_2
	s_sleep 127
	s_sleep 127
.Lstag_2:
	v_readlane_b32 s0, v254, 5
	s_andn2_b32 s0, s0, 63
	v_readlane_b32 s1, v254, 0
	s_cmpk_gt_i32 s1, 0x5ff
	s_mov_b32 s1, -1
	s_nop 0
	v_mbcnt_lo_u32_b32 v0, s1, 0
	v_mbcnt_hi_u32_b32 v0, s1, v0
	v_add_u32_e32 v8, s0, v0
	s_nop 0
	v_readfirstlane_b32 s5, v8
	s_cbranch_scc1 .LBB0_2059
	v_lshlrev_b32_e32 v0, 4, v8
	v_add_u32_e32 v1, 0x2000, v0
	v_ashrrev_i32_e32 v2, 31, v1
	v_lshrrev_b32_e32 v2, 22, v2
	v_add_u32_e32 v2, v1, v2
	v_ashrrev_i32_e32 v2, 10, v2
	v_mul_i32_i24_e32 v3, 0x400, v2
	v_sub_u32_e32 v1, v1, v3
	v_lshrrev_b32_e32 v3, 4, v1
	v_bitop3_b32 v1, v3, v1, 32 bitop3:0x6c
	v_ashrrev_i32_e32 v3, 31, v1
	v_lshrrev_b32_e32 v3, 26, v3
	v_add_u32_e32 v3, v1, v3
	s_waitcnt lgkmcnt(0)
	v_lshlrev_b32_e32 v5, 3, v2
	v_ashrrev_i32_e32 v4, 6, v3
	v_and_b32_e32 v5, -16, v5
	v_and_b32_e32 v3, 0xc0, v3
	v_add_u32_e32 v5, v4, v5
	v_and_b32_e32 v4, 3, v4
	s_mov_b32 s0, 0x3fffe0
	v_sub_u32_e32 v1, v1, v3
	v_mov_b32_e32 v3, 1
	v_and_or_b32 v4, v5, s0, v4
	v_lshrrev_b32_e32 v6, 2, v5
	v_lshlrev_b32_e32 v5, 1, v5
	v_lshlrev_b32_e32 v2, 5, v2
	v_ashrrev_i16_sdwa v1, v3, sext(v1) dst_sel:DWORD dst_unused:UNUSED_PAD src0_sel:DWORD src1_sel:BYTE_0
	v_and_b32_e32 v6, 4, v6
	v_and_b32_e32 v5, 24, v5
	v_and_b32_e32 v2, 32, v2
	v_bfe_i32 v1, v1, 0, 16
	v_or3_b32 v4, v4, v6, v5
	v_add_lshl_u32 v1, v2, v1, 1
	v_lshl_add_u32 v160, v4, 10, v1
	v_bfe_i32 v1, v8, 27, 1
	v_lshrrev_b32_e32 v1, 22, v1
	v_add_u32_e32 v1, v0, v1
	v_and_b32_e32 v1, 0xfffffc00, v1
	v_sub_u32_e32 v0, v0, v1
	v_lshrrev_b32_e32 v1, 4, v0
	v_ashrrev_i32_e32 v4, 31, v8
	v_bitop3_b32 v0, v1, v0, 32 bitop3:0x6c
	v_lshrrev_b32_e32 v4, 26, v4
	v_ashrrev_i32_e32 v1, 31, v0
	v_add_u32_e32 v4, v8, v4
	v_lshrrev_b32_e32 v1, 26, v1
	v_ashrrev_i32_e32 v4, 6, v4
	v_add_u32_e32 v1, v0, v1
	v_lshlrev_b32_e32 v5, 3, v4
	s_add_u32 s18, s90, 0x800000
	v_readlane_b32 s4, v254, 0
	v_ashrrev_i32_e32 v2, 6, v1
	v_and_b32_e32 v5, -16, v5
	v_and_b32_e32 v1, 0xc0, v1
	s_addc_u32 s19, s91, 0
	s_ashr_i32 s20, s4, 31
	v_add_u32_e32 v5, v2, v5
	v_and_b32_e32 v2, 3, v2
	v_sub_u32_e32 v0, v0, v1
	v_and_or_b32 v2, v5, s0, v2
	v_lshrrev_b32_e32 v6, 2, v5
	v_lshlrev_b32_e32 v5, 1, v5
	v_lshlrev_b32_e32 v4, 5, v4
	v_ashrrev_i16_sdwa v0, v3, sext(v0) dst_sel:DWORD dst_unused:UNUSED_PAD src0_sel:DWORD src1_sel:BYTE_0
	s_lshr_b32 s0, s20, 29
	v_and_b32_e32 v6, 4, v6
	v_and_b32_e32 v5, 24, v5
	v_and_b32_e32 v4, 32, v4
	v_bfe_i32 v0, v0, 0, 16
	s_add_i32 s0, s4, s0
	s_ashr_i32 s2, s5, 6
	v_or3_b32 v2, v2, v6, v5
	v_add_lshl_u32 v0, v4, v0, 1
	s_ashr_i32 s1, s0, 3
	s_and_b32 s0, s0, -8
	s_ashr_i32 s6, s5, 8
	s_lshl_b32 s3, s2, 10
	v_lshl_add_u32 v162, v2, 10, v0
	s_sub_i32 s0, s4, s0
	v_mov_b32_e32 v0, v8
	s_cmp_lt_i32 s0, 0
	s_movk_i32 s21, 0xc1
	s_cselect_b32 s4, s21, 0xc0
	v_ashrrev_i32_e32 v2, 31, v0
	v_lshrrev_b32_e32 v2, 26, v2
	s_mul_i32 s0, s4, s0
	v_lshlrev_b32_e32 v1, 4, v0
	v_add_u32_e32 v2, v0, v2
	v_bfe_i32 v0, v0, 27, 1
	s_add_i32 s0, s0, s1
	v_lshrrev_b32_e32 v0, 22, v0
	s_mul_hi_i32 s1, s0, 0x2aaaaaab
	v_add_u32_e32 v0, v1, v0
	s_lshr_b32 s4, s1, 31
	s_ashr_i32 s1, s1, 4
	v_and_b32_e32 v0, 0xfffffc00, v0
	s_add_i32 s1, s1, s4
	v_sub_u32_e32 v0, v1, v0
	s_lshl_b32 s7, s1, 3
	s_mulk_i32 s1, 0x60
	v_ashrrev_i32_e32 v9, 6, v2
	v_lshrrev_b32_e32 v2, 4, v0
	s_sub_i32 s0, s0, s1
	v_bitop3_b32 v0, v2, v0, 32 bitop3:0x6c
	s_bfe_i32 s1, s0, 0x80000
	v_ashrrev_i32_e32 v4, 31, v0
	s_bfe_u32 s1, s1, 0x3000c
	v_lshrrev_b32_e32 v4, 26, v4
	s_add_i32 s1, s0, s1
	v_add_u32_e32 v4, v0, v4
	s_bfe_i32 s4, s1, 0x80000
	s_and_b32 s1, s1, 0xf8
	v_ashrrev_i32_e32 v10, 6, v4
	v_and_b32_e32 v4, 0xc0, v4
	v_add_u32_e32 v1, 0x2000, v1
	s_sub_i32 s0, s0, s1
	v_sub_u32_e32 v0, v0, v4
	v_ashrrev_i32_e32 v4, 31, v1
	s_sext_i32_i16 s4, s4
	s_sext_i32_i8 s0, s0
	v_lshrrev_b32_e32 v4, 22, v4
	s_lshr_b32 s4, s4, 3
	s_add_i32 s16, s7, s0
	v_add_u32_e32 v4, v1, v4
	v_ashrrev_i32_e32 v12, 10, v4
	s_ashr_i32 s17, s16, 31
	s_bfe_i64 s[8:9], s[4:5], 0x100000
	v_mul_i32_i24_e32 v4, 0x400, v12
	s_lshl_b64 s[0:1], s[16:17], 18
	s_lshl_b64 s[8:9], s[8:9], 18
	v_sub_u32_e32 v1, v1, v4
	s_add_u32 s26, s18, s8
	v_lshlrev_b32_e32 v5, 5, v9
	v_ashrrev_i16_sdwa v0, v3, sext(v0) dst_sel:DWORD dst_unused:UNUSED_PAD src0_sel:DWORD src1_sel:BYTE_0
	v_lshrrev_b32_e32 v4, 4, v1
	s_addc_u32 s27, s19, s9
	s_add_i32 s17, s3, 0
	v_and_b32_e32 v5, 32, v5
	v_bfe_i32 v11, v0, 0, 16
	v_bitop3_b32 v1, v4, v1, 32 bitop3:0x6c
	s_add_i32 s22, s17, 0x10000
	s_add_i32 s23, s17, 0x12000
	v_add_u32_e32 v0, v5, v11
	v_ashrrev_i32_e32 v5, 31, v1
	s_mov_b32 m0, s22
	s_add_u32 s8, s26, 0x20000
	v_lshrrev_b32_e32 v5, 26, v5
	global_load_lds_dwordx4 v162, s[26:27]
	s_mov_b32 m0, s23
	s_addc_u32 s9, s27, 0
	s_add_i32 s30, s17, 0x14000
	v_add_u32_e32 v5, v1, v5
	global_load_lds_dwordx4 v160, s[26:27]
	s_mov_b32 m0, s30
	s_add_i32 s31, s17, 0x16000
	v_ashrrev_i32_e32 v13, 6, v5
	v_and_b32_e32 v5, 0xc0, v5
	global_load_lds_dwordx4 v162, s[8:9]
	s_mov_b32 m0, s31
	v_lshlrev_b32_e32 v2, 3, v9
	v_sub_u32_e32 v1, v1, v5
	global_load_lds_dwordx4 v160, s[8:9]
	v_readlane_b32 s8, v254, 44
	v_and_b32_e32 v2, 0x3ffff0, v2
	v_lshlrev_b32_e32 v4, 3, v12
	v_lshlrev_b32_e32 v6, 5, v12
	v_ashrrev_i16_sdwa v1, v3, sext(v1) dst_sel:DWORD dst_unused:UNUSED_PAD src0_sel:DWORD src1_sel:BYTE_0
	v_readlane_b32 s9, v254, 45
	s_add_u32 s24, s8, s0
	v_and_b32_e32 v4, 0x3ffff0, v4
	v_and_b32_e32 v6, 32, v6
	v_bfe_i32 v14, v1, 0, 16
	v_add_lshl_u32 v2, v10, v2, 10
	s_addc_u32 s25, s9, s1
	s_add_i32 s33, s17, 0x2000
	v_add_u32_e32 v1, v6, v14
	v_lshl_add_u32 v164, v0, 1, v2
	v_add_lshl_u32 v0, v13, v4, 10
	s_mov_b32 m0, s17
	s_add_u32 s0, s24, 0x20000
	v_lshl_add_u32 v166, v1, 1, v0
	global_load_lds_dwordx4 v164, s[24:25]
	s_mov_b32 m0, s33
	s_addc_u32 s1, s25, 0
	s_add_i32 s34, s17, 0x4000
	global_load_lds_dwordx4 v166, s[24:25]
	s_mov_b32 m0, s34
	s_add_i32 s35, s17, 0x6000
	global_load_lds_dwordx4 v164, s[0:1]
	s_mov_b32 m0, s35
	v_mov_b32_e32 v163, 0
	global_load_lds_dwordx4 v166, s[0:1]
	v_mov_b32_e32 v161, v163
	v_mov_b32_e32 v165, v163
	v_mov_b32_e32 v167, v163
	s_cmp_eq_u32 s6, 1
	v_lshl_add_u64 v[6:7], s[26:27], 0, v[162:163]
	v_lshl_add_u64 v[4:5], s[26:27], 0, v[160:161]
	v_lshl_add_u64 v[0:1], s[24:25], 0, v[164:165]
	s_cselect_b64 s[0:1], -1, 0
	s_cmp_lg_u32 s6, 1
	v_lshl_add_u64 v[2:3], s[24:25], 0, v[166:167]
	s_cbranch_scc1 .LBB0_2045
	s_barrier

.LBB0_2920:
	s_cmp_gt_i32 s12, 39
	s_cselect_b64 s[0:1], -1, 0
	s_cmp_lt_i32 s13, 31
	s_cselect_b64 s[2:3], -1, 0
	s_or_b64 s[0:1], s[0:1], s[2:3]
	s_and_b64 vcc, exec, s[0:1]
	v_readlane_b32 s83, v254, 0
	s_cbranch_vccnz .LBB0_3660
	s_add_u32 s0, s90, 0x380000
	s_mov_b64 s[84:85], s[12:13]
	s_addc_u32 s1, s91, 0
	s_cmp_lt_i32 s84, 32
	s_cselect_b64 s[2:3], -1, 0
	s_cmp_gt_u32 s85, 31
	s_cselect_b64 s[4:5], -1, 0
	s_and_b64 s[2:3], s[2:3], s[4:5]
	v_readlane_b32 s86, v254, 50
	s_andn2_b64 vcc, exec, s[2:3]
	v_readlane_b32 s87, v254, 51
	s_cbranch_vccnz .LBB0_2997
	v_readlane_b32 s32, v254, 0
	s_nop 3
	s_bitcmp1_b32 s32, 2
	s_cbranch_scc0 .Lstag_3
	s_sleep 127
	s_sleep 127
.Lstag_3:
	s_mov_b32 s3, -1
	v_readlane_b32 s2, v254, 5
	s_andn2_b32 s2, s2, 63
	v_mbcnt_lo_u32_b32 v0, s3, 0
	v_mbcnt_hi_u32_b32 v0, s3, v0
	v_add_u32_e32 v8, s2, v0
	s_cmpk_gt_i32 s83, 0x5ff
	s_nop 0
	v_readfirstlane_b32 s3, v8
	s_cbranch_scc1 .LBB0_2943
	v_lshlrev_b32_e32 v0, 4, v8
	v_add_u32_e32 v1, 0x2000, v0
	v_ashrrev_i32_e32 v2, 31, v1
	v_lshrrev_b32_e32 v2, 22, v2
	v_add_u32_e32 v2, v1, v2
	v_ashrrev_i32_e32 v2, 10, v2
	v_mul_i32_i24_e32 v3, 0x400, v2
	v_sub_u32_e32 v1, v1, v3
	v_lshrrev_b32_e32 v3, 4, v1
	v_bitop3_b32 v1, v3, v1, 32 bitop3:0x6c
	v_ashrrev_i32_e32 v3, 31, v1
	v_lshrrev_b32_e32 v3, 26, v3
	v_add_u32_e32 v3, v1, v3
	s_waitcnt lgkmcnt(0)
	v_lshlrev_b32_e32 v5, 3, v2
	v_ashrrev_i32_e32 v4, 6, v3
	v_and_b32_e32 v5, -16, v5
	v_and_b32_e32 v3, 0xc0, v3
	v_add_u32_e32 v5, v4, v5
	v_and_b32_e32 v4, 3, v4
	s_mov_b32 s2, 0x3fffe0
	v_sub_u32_e32 v1, v1, v3
	v_mov_b32_e32 v3, 1
	v_and_or_b32 v4, v5, s2, v4
	v_lshrrev_b32_e32 v6, 2, v5
	v_lshlrev_b32_e32 v5, 1, v5
	v_lshlrev_b32_e32 v2, 5, v2
	v_ashrrev_i16_sdwa v1, v3, sext(v1) dst_sel:DWORD dst_unused:UNUSED_PAD src0_sel:DWORD src1_sel:BYTE_0
	v_and_b32_e32 v6, 4, v6
	v_and_b32_e32 v5, 24, v5
	v_and_b32_e32 v2, 32, v2
	v_bfe_i32 v1, v1, 0, 16
	v_or3_b32 v4, v4, v6, v5
	v_add_lshl_u32 v1, v2, v1, 1
	v_lshl_add_u32 v160, v4, 10, v1
	v_bfe_i32 v1, v8, 27, 1
	v_lshrrev_b32_e32 v1, 22, v1
	v_add_u32_e32 v1, v0, v1
	v_and_b32_e32 v1, 0xfffffc00, v1
	v_sub_u32_e32 v0, v0, v1
	v_lshrrev_b32_e32 v1, 4, v0
	v_ashrrev_i32_e32 v4, 31, v8
	v_bitop3_b32 v0, v1, v0, 32 bitop3:0x6c
	v_lshrrev_b32_e32 v4, 26, v4
	v_ashrrev_i32_e32 v1, 31, v0
	v_add_u32_e32 v4, v8, v4
	v_lshrrev_b32_e32 v1, 26, v1
	v_ashrrev_i32_e32 v4, 6, v4
	v_add_u32_e32 v1, v0, v1
	v_lshlrev_b32_e32 v5, 3, v4
	s_add_u32 s28, s90, 0x2c500000
	v_ashrrev_i32_e32 v2, 6, v1
	v_and_b32_e32 v5, -16, v5
	v_and_b32_e32 v1, 0xc0, v1
	s_addc_u32 s29, s91, 0
	s_ashr_i32 s30, s83, 31
	v_add_u32_e32 v5, v2, v5
	v_and_b32_e32 v2, 3, v2
	v_sub_u32_e32 v0, v0, v1
	v_and_or_b32 v2, v5, s2, v2
	v_lshrrev_b32_e32 v6, 2, v5
	v_lshlrev_b32_e32 v5, 1, v5
	v_lshlrev_b32_e32 v4, 5, v4
	v_ashrrev_i16_sdwa v0, v3, sext(v0) dst_sel:DWORD dst_unused:UNUSED_PAD src0_sel:DWORD src1_sel:BYTE_0
	s_lshr_b32 s2, s30, 29
	v_and_b32_e32 v6, 4, v6
	v_and_b32_e32 v5, 24, v5
	v_and_b32_e32 v4, 32, v4
	v_bfe_i32 v0, v0, 0, 16
	s_add_i32 s2, s83, s2
	s_ashr_i32 s8, s3, 6
	v_or3_b32 v2, v2, v6, v5
	v_add_lshl_u32 v0, v4, v0, 1
	s_ashr_i32 s4, s2, 3
	s_and_b32 s2, s2, -8
	s_ashr_i32 s10, s3, 8
	s_lshl_b32 s9, s8, 10
	v_lshl_add_u32 v162, v2, 10, v0
	s_sub_i32 s2, s83, s2
	v_mov_b32_e32 v0, v8
	s_cmp_lt_i32 s2, 0
	s_movk_i32 s31, 0xc1
	s_cselect_b32 s5, s31, 0xc0
	v_ashrrev_i32_e32 v2, 31, v0
	v_lshrrev_b32_e32 v2, 26, v2
	s_mul_i32 s2, s5, s2
	v_lshlrev_b32_e32 v1, 4, v0
	v_add_u32_e32 v2, v0, v2
	v_bfe_i32 v0, v0, 27, 1
	s_add_i32 s2, s2, s4
	v_lshrrev_b32_e32 v0, 22, v0
	s_mul_hi_i32 s4, s2, 0x2aaaaaab
	v_add_u32_e32 v0, v1, v0
	s_lshr_b32 s5, s4, 31
	s_ashr_i32 s4, s4, 4
	v_and_b32_e32 v0, 0xfffffc00, v0
	s_add_i32 s4, s4, s5
	v_sub_u32_e32 v0, v1, v0
	s_lshl_b32 s5, s4, 3
	s_mulk_i32 s4, 0x60
	v_ashrrev_i32_e32 v9, 6, v2
	v_lshrrev_b32_e32 v2, 4, v0
	s_sub_i32 s4, s2, s4
	v_bitop3_b32 v0, v2, v0, 32 bitop3:0x6c
	s_bfe_i32 s2, s4, 0x80000
	v_ashrrev_i32_e32 v4, 31, v0
	s_bfe_u32 s2, s2, 0x3000c
	v_lshrrev_b32_e32 v4, 26, v4
	s_add_i32 s6, s4, s2
	v_add_u32_e32 v4, v0, v4
	s_bfe_i32 s2, s6, 0x80000
	s_and_b32 s6, s6, 0xf8
	v_ashrrev_i32_e32 v10, 6, v4
	v_and_b32_e32 v4, 0xc0, v4
	v_add_u32_e32 v1, 0x2000, v1
	s_sub_i32 s4, s4, s6
	v_sub_u32_e32 v0, v0, v4
	v_ashrrev_i32_e32 v4, 31, v1
	s_sext_i32_i16 s2, s2
	s_sext_i32_i8 s4, s4
	v_lshrrev_b32_e32 v4, 22, v4
	s_lshr_b32 s2, s2, 3
	s_add_i32 s4, s5, s4
	v_add_u32_e32 v4, v1, v4
	v_ashrrev_i32_e32 v12, 10, v4
	s_ashr_i32 s5, s4, 31
	s_bfe_i64 s[12:13], s[2:3], 0x100000
	v_mul_i32_i24_e32 v4, 0x400, v12
	s_lshl_b64 s[6:7], s[4:5], 18
	s_lshl_b64 s[12:13], s[12:13], 18
	v_sub_u32_e32 v1, v1, v4
	s_add_u32 s24, s28, s12
	v_lshlrev_b32_e32 v5, 5, v9
	v_ashrrev_i16_sdwa v0, v3, sext(v0) dst_sel:DWORD dst_unused:UNUSED_PAD src0_sel:DWORD src1_sel:BYTE_0
	v_lshrrev_b32_e32 v4, 4, v1
	s_addc_u32 s25, s29, s13
	s_add_i32 s33, s9, 0
	v_and_b32_e32 v5, 32, v5
	v_bfe_i32 v11, v0, 0, 16
	v_bitop3_b32 v1, v4, v1, 32 bitop3:0x6c
	s_add_i32 s34, s33, 0x10000
	s_add_i32 s35, s33, 0x12000
	v_add_u32_e32 v0, v5, v11
	v_ashrrev_i32_e32 v5, 31, v1
	s_mov_b32 m0, s34
	s_add_u32 s12, s24, 0x20000
	v_lshrrev_b32_e32 v5, 26, v5
	global_load_lds_dwordx4 v162, s[24:25]
	s_mov_b32 m0, s35
	s_addc_u32 s13, s25, 0
	s_add_i32 s36, s33, 0x14000
	v_add_u32_e32 v5, v1, v5
	global_load_lds_dwordx4 v160, s[24:25]
	s_mov_b32 m0, s36
	s_add_i32 s37, s33, 0x16000
	v_ashrrev_i32_e32 v13, 6, v5
	v_and_b32_e32 v5, 0xc0, v5
	global_load_lds_dwordx4 v162, s[12:13]
	s_mov_b32 m0, s37
	v_lshlrev_b32_e32 v2, 3, v9
	v_sub_u32_e32 v1, v1, v5
	global_load_lds_dwordx4 v160, s[12:13]
	v_readlane_b32 s12, v254, 44
	v_and_b32_e32 v2, 0x3ffff0, v2
	v_lshlrev_b32_e32 v4, 3, v12
	v_lshlrev_b32_e32 v6, 5, v12
	v_ashrrev_i16_sdwa v1, v3, sext(v1) dst_sel:DWORD dst_unused:UNUSED_PAD src0_sel:DWORD src1_sel:BYTE_0
	v_readlane_b32 s13, v254, 45
	s_add_u32 s22, s12, s6
	v_and_b32_e32 v4, 0x3ffff0, v4
	v_and_b32_e32 v6, 32, v6
	v_bfe_i32 v14, v1, 0, 16
	v_add_lshl_u32 v2, v10, v2, 10
	s_addc_u32 s23, s13, s7
	s_add_i32 s38, s33, 0x2000
	v_add_u32_e32 v1, v6, v14
	v_lshl_add_u32 v164, v0, 1, v2
	v_add_lshl_u32 v0, v13, v4, 10
	s_mov_b32 m0, s33
	s_add_u32 s6, s22, 0x20000
	v_lshl_add_u32 v166, v1, 1, v0
	global_load_lds_dwordx4 v164, s[22:23]
	s_mov_b32 m0, s38
	s_addc_u32 s7, s23, 0
	s_add_i32 s39, s33, 0x4000
	global_load_lds_dwordx4 v166, s[22:23]
	s_mov_b32 m0, s39
	s_add_i32 s40, s33, 0x6000
	global_load_lds_dwordx4 v164, s[6:7]
	s_mov_b32 m0, s40
	v_mov_b32_e32 v163, 0
	global_load_lds_dwordx4 v166, s[6:7]
	v_mov_b32_e32 v161, v163
	v_mov_b32_e32 v165, v163
	v_mov_b32_e32 v167, v163
	s_cmp_eq_u32 s10, 1
	v_lshl_add_u64 v[6:7], s[24:25], 0, v[162:163]
	v_lshl_add_u64 v[4:5], s[24:25], 0, v[160:161]
	v_lshl_add_u64 v[0:1], s[22:23], 0, v[164:165]
	s_cselect_b64 s[6:7], -1, 0
	s_cmp_lg_u32 s10, 1
	v_lshl_add_u64 v[2:3], s[22:23], 0, v[166:167]
	s_cbranch_scc1 .LBB0_2925
	s_barrier
